# k_f3 + MoE-up: leading half's epilogue-align barrier moved 3 groups into the epilogue (its first 3 groups overlap the trailing half's last MFMA segment)
# speedup vs baseline: 1.0008x; 1.0008x over previous
; __device__ __forceinline__ float silu_f(float x) { return x * __builtin_amdgcn_rcpf(1.0f + __builtin_amdgcn_exp2f(-1.4426950409f * x)); }
; #define PG8_BAR __builtin_amdgcn_s_barrier()
;     __device__ __forceinline__ void operator()(const f32x4 (&acc)[2][2][4][2], const Unit& u, int wr, int wc, int fr, int fq) const {
;     ...
;         const int row0 = u.pm * BM + wr * 64 + fr, col0 = u.pn * HALF + wc * 32 + 8 * fq;
; #pragma unroll
;         for (int ai = 0; ai < 2; ++ai)
; #pragma unroll
;             for (int m = 0; m < 4; ++m) {
;                 const float r = rs[ai][m]; f32x4 o[2];
; #pragma unroll
;                 for (int n = 0; n < 2; ++n) { const f32x4 a = acc[ai][0][m][n] * r, b = acc[ai][1][m][n] * r;
;                     o[n] = (f32x4){silu_f(a[0]) * b[0], silu_f(a[1]) * b[1], silu_f(a[2]) * b[2], silu_f(a[3]) * b[3]}; }
;                 if (F8OUT) { u32x2 w; w.x = pack4_fp8(o[0]); w.y = pack4_fp8(o[1]); *(u32x2*)((unsigned char*)h + (size_t)(row0 + ai * HALF + m * 16) * FFN + col0) = w; }
; template <class Epi, class Sched, bool ALIGN_EPI = false, bool SP2 = false, bool F8 = false>
; __device__ __forceinline__ void gemm_phase(PG8_LAS unsigned char* lds, const Gemm g, const Sched& S, const Epi& E, const int tidb  ) {
;     ...
;         if constexpr (ALIGN_EPI) { if (wr == 0) PG8_BAR; }
;         if constexpr (F8) asm volatile("s_nop 15\n\ts_nop 15" ::: "memory");
;         if constexpr (!Epi::AFTER_DRAIN) { E(acc, cur, wr, wc, fr, fq); S.done(cur); }
.LBB0_1373:
.LBB0_1375:
	v_mov_b32_e32 v14, 0xbfb8aa3b
	v_mov_b32_e32 v20, 1.0
	v_pk_mul_f32 v[4:5], v[154:155], v[14:15] op_sel_hi:[1,0]
	v_pk_mul_f32 v[6:7], v[156:157], v[14:15] op_sel_hi:[1,0]
	v_pk_mul_f32 v[8:9], v[150:151], v[14:15] op_sel_hi:[1,0]
	v_pk_mul_f32 v[10:11], v[152:153], v[14:15] op_sel_hi:[1,0]
	v_exp_f32_e32 v4, v4
	v_exp_f32_e32 v5, v5
	v_exp_f32_e32 v6, v6
	v_exp_f32_e32 v7, v7
	v_exp_f32_e32 v8, v8
	v_exp_f32_e32 v9, v9
	v_exp_f32_e32 v10, v10
	v_exp_f32_e32 v11, v11
	v_pk_add_f32 v[4:5], v[4:5], v[20:21] op_sel_hi:[1,0]
	v_pk_add_f32 v[6:7], v[6:7], v[20:21] op_sel_hi:[1,0]
	v_pk_add_f32 v[8:9], v[8:9], v[20:21] op_sel_hi:[1,0]
	v_pk_add_f32 v[10:11], v[10:11], v[20:21] op_sel_hi:[1,0]
	v_rcp_f32_e32 v4, v4
	v_rcp_f32_e32 v5, v5
	v_rcp_f32_e32 v6, v6
	v_rcp_f32_e32 v7, v7
	v_rcp_f32_e32 v8, v8
	v_rcp_f32_e32 v9, v9
	v_rcp_f32_e32 v10, v10
	v_rcp_f32_e32 v11, v11
	v_pk_mul_f32 v[4:5], v[154:155], v[4:5]
	v_pk_mul_f32 v[6:7], v[156:157], v[6:7]
	v_pk_mul_f32 v[8:9], v[150:151], v[8:9]
	v_pk_mul_f32 v[10:11], v[152:153], v[10:11]
	v_pk_mul_f32 v[4:5], v[158:159], v[4:5]
	v_pk_mul_f32 v[6:7], v[160:161], v[6:7]
	v_pk_mul_f32 v[8:9], v[146:147], v[8:9]
	v_pk_mul_f32 v[10:11], v[148:149], v[10:11]
	v_med3_f32 v4, v4, s64, v250
	v_med3_f32 v5, v5, s64, v250
	v_med3_f32 v6, v6, s64, v250
	v_med3_f32 v7, v7, s64, v250
	v_med3_f32 v8, v8, s64, v250
	v_med3_f32 v9, v9, s64, v250
	v_med3_f32 v10, v10, s64, v250
	v_med3_f32 v11, v11, s64, v250
	v_cvt_pk_fp8_f32 v12, v4, v5
	v_cvt_pk_fp8_f32 v13, v8, v9
	s_nop 0
	v_cvt_pk_fp8_f32 v12, v6, v7 op_sel:[0,0,1]
	v_cvt_pk_fp8_f32 v13, v10, v11 op_sel:[0,0,1]
	v_lshl_or_b32 v2, s62, 7, v193
	v_ashrrev_i32_e32 v3, 31, v2
	v_lshl_add_u32 v0, s63, 8, v163
	v_lshl_add_u64 v[2:3], s[20:21], 0, v[2:3]
	s_nop 15
	s_nop 15
	v_mad_i64_i32 v[18:19], s[22:23], v0, s73, v[2:3]
	s_waitcnt vmcnt(0)
	global_store_dwordx2 v[18:19], v[12:13], off
	v_pk_mul_f32 v[4:5], v[142:143], v[14:15] op_sel_hi:[1,0]
	v_pk_mul_f32 v[6:7], v[144:145], v[14:15] op_sel_hi:[1,0]
	v_pk_mul_f32 v[8:9], v[134:135], v[14:15] op_sel_hi:[1,0]
	v_pk_mul_f32 v[10:11], v[136:137], v[14:15] op_sel_hi:[1,0]
	v_exp_f32_e32 v4, v4
	v_exp_f32_e32 v5, v5
	v_exp_f32_e32 v6, v6
	v_exp_f32_e32 v7, v7
	v_exp_f32_e32 v8, v8
	v_exp_f32_e32 v9, v9
	v_exp_f32_e32 v10, v10
	v_exp_f32_e32 v11, v11
	v_pk_add_f32 v[4:5], v[4:5], v[20:21] op_sel_hi:[1,0]
	v_pk_add_f32 v[6:7], v[6:7], v[20:21] op_sel_hi:[1,0]
	v_pk_add_f32 v[8:9], v[8:9], v[20:21] op_sel_hi:[1,0]
	v_pk_add_f32 v[10:11], v[10:11], v[20:21] op_sel_hi:[1,0]
	v_rcp_f32_e32 v4, v4
	v_rcp_f32_e32 v5, v5
	v_rcp_f32_e32 v6, v6
	v_rcp_f32_e32 v7, v7
	v_rcp_f32_e32 v8, v8
	v_rcp_f32_e32 v9, v9
	v_rcp_f32_e32 v10, v10
	v_rcp_f32_e32 v11, v11
	v_pk_mul_f32 v[4:5], v[142:143], v[4:5]
	v_pk_mul_f32 v[6:7], v[144:145], v[6:7]
	v_pk_mul_f32 v[8:9], v[134:135], v[8:9]
	v_pk_mul_f32 v[10:11], v[136:137], v[10:11]
	v_pk_mul_f32 v[4:5], v[138:139], v[4:5]
	v_pk_mul_f32 v[6:7], v[140:141], v[6:7]
	v_pk_mul_f32 v[8:9], v[130:131], v[8:9]
	v_pk_mul_f32 v[10:11], v[132:133], v[10:11]
	v_med3_f32 v4, v4, s64, v250
	v_med3_f32 v5, v5, s64, v250
	v_med3_f32 v6, v6, s64, v250
	v_med3_f32 v7, v7, s64, v250
	v_med3_f32 v8, v8, s64, v250
	v_med3_f32 v9, v9, s64, v250
	v_med3_f32 v10, v10, s64, v250
	v_med3_f32 v11, v11, s64, v250
	v_cvt_pk_fp8_f32 v12, v4, v5
	v_cvt_pk_fp8_f32 v13, v8, v9
	s_nop 0
	v_cvt_pk_fp8_f32 v12, v6, v7 op_sel:[0,0,1]
	v_cvt_pk_fp8_f32 v13, v10, v11 op_sel:[0,0,1]
	v_or_b32_e32 v18, 16, v0
	v_mad_i64_i32 v[18:19], s[22:23], v18, s73, v[2:3]
	global_store_dwordx2 v[18:19], v[12:13], off
	v_pk_mul_f32 v[4:5], v[126:127], v[14:15] op_sel_hi:[1,0]
	v_pk_mul_f32 v[6:7], v[128:129], v[14:15] op_sel_hi:[1,0]
	v_pk_mul_f32 v[8:9], v[118:119], v[14:15] op_sel_hi:[1,0]
	v_pk_mul_f32 v[10:11], v[120:121], v[14:15] op_sel_hi:[1,0]
	v_exp_f32_e32 v4, v4
	v_exp_f32_e32 v5, v5
	v_exp_f32_e32 v6, v6
	v_exp_f32_e32 v7, v7
	v_exp_f32_e32 v8, v8
	v_exp_f32_e32 v9, v9
	v_exp_f32_e32 v10, v10
	v_exp_f32_e32 v11, v11
	v_pk_add_f32 v[4:5], v[4:5], v[20:21] op_sel_hi:[1,0]
	v_pk_add_f32 v[6:7], v[6:7], v[20:21] op_sel_hi:[1,0]
	v_pk_add_f32 v[8:9], v[8:9], v[20:21] op_sel_hi:[1,0]
	v_pk_add_f32 v[10:11], v[10:11], v[20:21] op_sel_hi:[1,0]
	v_rcp_f32_e32 v4, v4
	v_rcp_f32_e32 v5, v5
	v_rcp_f32_e32 v6, v6
	v_rcp_f32_e32 v7, v7
	v_rcp_f32_e32 v8, v8
	v_rcp_f32_e32 v9, v9
	v_rcp_f32_e32 v10, v10
	v_rcp_f32_e32 v11, v11
	v_pk_mul_f32 v[4:5], v[126:127], v[4:5]
	v_pk_mul_f32 v[6:7], v[128:129], v[6:7]
	v_pk_mul_f32 v[8:9], v[118:119], v[8:9]
	v_pk_mul_f32 v[10:11], v[120:121], v[10:11]
	v_pk_mul_f32 v[4:5], v[122:123], v[4:5]
	v_pk_mul_f32 v[6:7], v[124:125], v[6:7]
	v_pk_mul_f32 v[8:9], v[114:115], v[8:9]
	v_pk_mul_f32 v[10:11], v[116:117], v[10:11]
	v_med3_f32 v4, v4, s64, v250
	v_med3_f32 v5, v5, s64, v250
	v_med3_f32 v6, v6, s64, v250
	v_med3_f32 v7, v7, s64, v250
	v_med3_f32 v8, v8, s64, v250
	v_med3_f32 v9, v9, s64, v250
	v_med3_f32 v10, v10, s64, v250
	v_med3_f32 v11, v11, s64, v250
	v_cvt_pk_fp8_f32 v12, v4, v5
	v_cvt_pk_fp8_f32 v13, v8, v9
	s_nop 0
	v_cvt_pk_fp8_f32 v12, v6, v7 op_sel:[0,0,1]
	v_cvt_pk_fp8_f32 v13, v10, v11 op_sel:[0,0,1]
	v_or_b32_e32 v18, 32, v0
	v_mad_i64_i32 v[18:19], s[22:23], v18, s73, v[2:3]
	global_store_dwordx2 v[18:19], v[12:13], off
	s_cmp_eq_u64 s[18:19], 0
	s_cbranch_scc1 .Lmoe_up_noalign
	s_barrier
; __device__ __forceinline__ float silu_f(float x) { return x * __builtin_amdgcn_rcpf(1.0f + __builtin_amdgcn_exp2f(-1.4426950409f * x)); }
;     __device__ __forceinline__ void operator()(const f32x4 (&acc)[2][2][4][2], const Unit& u, int wr, int wc, int fr, int fq) const {
;     ...
;         const int row0 = u.pm * BM + wr * 64 + fr, col0 = u.pn * HALF + wc * 32 + 8 * fq;
; #pragma unroll
;         for (int ai = 0; ai < 2; ++ai)
; #pragma unroll
;             for (int m = 0; m < 4; ++m) {
;                 const float r = rs[ai][m]; f32x4 o[2];
; #pragma unroll
;                 for (int n = 0; n < 2; ++n) { const f32x4 a = acc[ai][0][m][n] * r, b = acc[ai][1][m][n] * r;
;                     o[n] = (f32x4){silu_f(a[0]) * b[0], silu_f(a[1]) * b[1], silu_f(a[2]) * b[2], silu_f(a[3]) * b[3]}; }
;                 if (F8OUT) { u32x2 w; w.x = pack4_fp8(o[0]); w.y = pack4_fp8(o[1]); *(u32x2*)((unsigned char*)h + (size_t)(row0 + ai * HALF + m * 16) * FFN + col0) = w; }
.Lmoe_up_noalign:
	v_pk_mul_f32 v[4:5], v[110:111], v[14:15] op_sel_hi:[1,0]
	v_pk_mul_f32 v[6:7], v[112:113], v[14:15] op_sel_hi:[1,0]
	v_pk_mul_f32 v[8:9], v[102:103], v[14:15] op_sel_hi:[1,0]
	v_pk_mul_f32 v[10:11], v[104:105], v[14:15] op_sel_hi:[1,0]
	v_exp_f32_e32 v4, v4
	v_exp_f32_e32 v5, v5
	v_exp_f32_e32 v6, v6
	v_exp_f32_e32 v7, v7
	v_exp_f32_e32 v8, v8
	v_exp_f32_e32 v9, v9
	v_exp_f32_e32 v10, v10
	v_exp_f32_e32 v11, v11
	v_pk_add_f32 v[4:5], v[4:5], v[20:21] op_sel_hi:[1,0]
	v_pk_add_f32 v[6:7], v[6:7], v[20:21] op_sel_hi:[1,0]
	v_pk_add_f32 v[8:9], v[8:9], v[20:21] op_sel_hi:[1,0]
	v_pk_add_f32 v[10:11], v[10:11], v[20:21] op_sel_hi:[1,0]
	v_rcp_f32_e32 v4, v4
	v_rcp_f32_e32 v5, v5
	v_rcp_f32_e32 v6, v6
	v_rcp_f32_e32 v7, v7
	v_rcp_f32_e32 v8, v8
	v_rcp_f32_e32 v9, v9
	v_rcp_f32_e32 v10, v10
	v_rcp_f32_e32 v11, v11
	v_pk_mul_f32 v[4:5], v[110:111], v[4:5]
	v_pk_mul_f32 v[6:7], v[112:113], v[6:7]
	v_pk_mul_f32 v[8:9], v[102:103], v[8:9]
	v_pk_mul_f32 v[10:11], v[104:105], v[10:11]
	v_pk_mul_f32 v[4:5], v[106:107], v[4:5]
	v_pk_mul_f32 v[6:7], v[108:109], v[6:7]
	v_pk_mul_f32 v[8:9], v[98:99], v[8:9]
	v_pk_mul_f32 v[10:11], v[100:101], v[10:11]
	v_med3_f32 v4, v4, s64, v250
	v_med3_f32 v5, v5, s64, v250
	v_med3_f32 v6, v6, s64, v250
	v_med3_f32 v7, v7, s64, v250
	v_med3_f32 v8, v8, s64, v250
	v_med3_f32 v9, v9, s64, v250
	v_med3_f32 v10, v10, s64, v250
	v_med3_f32 v11, v11, s64, v250
	v_cvt_pk_fp8_f32 v12, v4, v5
	v_cvt_pk_fp8_f32 v13, v8, v9
	s_nop 0
	v_cvt_pk_fp8_f32 v12, v6, v7 op_sel:[0,0,1]
	v_cvt_pk_fp8_f32 v13, v10, v11 op_sel:[0,0,1]
	v_or_b32_e32 v18, 48, v0
	v_mad_i64_i32 v[18:19], s[22:23], v18, s73, v[2:3]
	global_store_dwordx2 v[18:19], v[12:13], off
	v_pk_mul_f32 v[4:5], v[94:95], v[14:15] op_sel_hi:[1,0]
	v_pk_mul_f32 v[6:7], v[96:97], v[14:15] op_sel_hi:[1,0]
	v_pk_mul_f32 v[8:9], v[86:87], v[14:15] op_sel_hi:[1,0]
	v_pk_mul_f32 v[10:11], v[88:89], v[14:15] op_sel_hi:[1,0]
	v_exp_f32_e32 v4, v4
	v_exp_f32_e32 v5, v5
	v_exp_f32_e32 v6, v6
	v_exp_f32_e32 v7, v7
	v_exp_f32_e32 v8, v8
	v_exp_f32_e32 v9, v9
	v_exp_f32_e32 v10, v10
	v_exp_f32_e32 v11, v11
	v_pk_add_f32 v[4:5], v[4:5], v[20:21] op_sel_hi:[1,0]
	v_pk_add_f32 v[6:7], v[6:7], v[20:21] op_sel_hi:[1,0]
	v_pk_add_f32 v[8:9], v[8:9], v[20:21] op_sel_hi:[1,0]
	v_pk_add_f32 v[10:11], v[10:11], v[20:21] op_sel_hi:[1,0]
	v_rcp_f32_e32 v4, v4
	v_rcp_f32_e32 v5, v5
	v_rcp_f32_e32 v6, v6
	v_rcp_f32_e32 v7, v7
	v_rcp_f32_e32 v8, v8
	v_rcp_f32_e32 v9, v9
	v_rcp_f32_e32 v10, v10
	v_rcp_f32_e32 v11, v11
	v_pk_mul_f32 v[4:5], v[94:95], v[4:5]
	v_pk_mul_f32 v[6:7], v[96:97], v[6:7]
	v_pk_mul_f32 v[8:9], v[86:87], v[8:9]
	v_pk_mul_f32 v[10:11], v[88:89], v[10:11]
	v_pk_mul_f32 v[4:5], v[90:91], v[4:5]
	v_pk_mul_f32 v[6:7], v[92:93], v[6:7]
	v_pk_mul_f32 v[8:9], v[82:83], v[8:9]
	v_pk_mul_f32 v[10:11], v[84:85], v[10:11]
	v_med3_f32 v4, v4, s64, v250
	v_med3_f32 v5, v5, s64, v250
	v_med3_f32 v6, v6, s64, v250
	v_med3_f32 v7, v7, s64, v250
	v_med3_f32 v8, v8, s64, v250
	v_med3_f32 v9, v9, s64, v250
	v_med3_f32 v10, v10, s64, v250
	v_med3_f32 v11, v11, s64, v250
	v_cvt_pk_fp8_f32 v12, v4, v5
	v_cvt_pk_fp8_f32 v13, v8, v9
	s_nop 0
	v_cvt_pk_fp8_f32 v12, v6, v7 op_sel:[0,0,1]
	v_cvt_pk_fp8_f32 v13, v10, v11 op_sel:[0,0,1]
	v_add_u32_e32 v18, 0x80, v0
	v_mad_i64_i32 v[18:19], s[22:23], v18, s73, v[2:3]
	global_store_dwordx2 v[18:19], v[12:13], off
	v_pk_mul_f32 v[4:5], v[78:79], v[14:15] op_sel_hi:[1,0]
	v_pk_mul_f32 v[6:7], v[80:81], v[14:15] op_sel_hi:[1,0]
	v_pk_mul_f32 v[8:9], v[70:71], v[14:15] op_sel_hi:[1,0]
	v_pk_mul_f32 v[10:11], v[72:73], v[14:15] op_sel_hi:[1,0]
	v_exp_f32_e32 v4, v4
	v_exp_f32_e32 v5, v5
	v_exp_f32_e32 v6, v6
	v_exp_f32_e32 v7, v7
	v_exp_f32_e32 v8, v8
	v_exp_f32_e32 v9, v9
	v_exp_f32_e32 v10, v10
	v_exp_f32_e32 v11, v11
	v_pk_add_f32 v[4:5], v[4:5], v[20:21] op_sel_hi:[1,0]
	v_pk_add_f32 v[6:7], v[6:7], v[20:21] op_sel_hi:[1,0]
	v_pk_add_f32 v[8:9], v[8:9], v[20:21] op_sel_hi:[1,0]
	v_pk_add_f32 v[10:11], v[10:11], v[20:21] op_sel_hi:[1,0]
	v_rcp_f32_e32 v4, v4
	v_rcp_f32_e32 v5, v5
	v_rcp_f32_e32 v6, v6
	v_rcp_f32_e32 v7, v7
	v_rcp_f32_e32 v8, v8
	v_rcp_f32_e32 v9, v9
	v_rcp_f32_e32 v10, v10
	v_rcp_f32_e32 v11, v11
	v_pk_mul_f32 v[4:5], v[78:79], v[4:5]
	v_pk_mul_f32 v[6:7], v[80:81], v[6:7]
; __device__ __forceinline__ float silu_f(float x) { return x * __builtin_amdgcn_rcpf(1.0f + __builtin_amdgcn_exp2f(-1.4426950409f * x)); }
; #define PG8_BAR __builtin_amdgcn_s_barrier()
;     __device__ __forceinline__ void operator()(const f32x4 (&acc)[2][2][4][2], const Unit& u, int wr, int wc, int fr, int fq) const {
;     ...
;         const int row0 = u.pm * BM + wr * 64 + fr, col0 = u.pn * HALF + wc * 32 + 8 * fq;
; #pragma unroll
;         for (int ai = 0; ai < 2; ++ai)
; #pragma unroll
;             for (int m = 0; m < 4; ++m) {
;                 const float r = rs[ai][m]; f32x4 o[2];
; #pragma unroll
;                 for (int n = 0; n < 2; ++n) { const f32x4 a = acc[ai][0][m][n] * r, b = acc[ai][1][m][n] * r;
;                     o[n] = (f32x4){silu_f(a[0]) * b[0], silu_f(a[1]) * b[1], silu_f(a[2]) * b[2], silu_f(a[3]) * b[3]}; }
;                 if (F8OUT) { u32x2 w; w.x = pack4_fp8(o[0]); w.y = pack4_fp8(o[1]); *(u32x2*)((unsigned char*)h + (size_t)(row0 + ai * HALF + m * 16) * FFN + col0) = w; }
; template <class Epi, class Sched, bool ALIGN_EPI = false, bool SP2 = false, bool F8 = false>
; __device__ __forceinline__ void gemm_phase(PG8_LAS unsigned char* lds, const Gemm g, const Sched& S, const Epi& E, const int tidb  ) {
;     ...
;         if (!has_next) break;
; #pragma unroll
;         for (int a = 0; a < 2; ++a)
; #pragma unroll
;             for (int b = 0; b < 2; ++b)
; #pragma unroll
;                 for (int m = 0; m < 4; ++m)
; #pragma unroll
;                     for (int n = 0; n < 2; ++n) acc[a][b][m][n] = (f32x4){0.f, 0.f, 0.f, 0.f};
;         cur = nxt; cA = nA; cB = nB; ++ui;
;         if constexpr (ALIGN_EPI) { if (wr == 1) PG8_BAR; }
	v_pk_mul_f32 v[8:9], v[70:71], v[8:9]
	v_pk_mul_f32 v[10:11], v[72:73], v[10:11]
	v_pk_mul_f32 v[4:5], v[74:75], v[4:5]
	v_pk_mul_f32 v[6:7], v[76:77], v[6:7]
	v_pk_mul_f32 v[8:9], v[66:67], v[8:9]
	v_pk_mul_f32 v[10:11], v[68:69], v[10:11]
	v_med3_f32 v4, v4, s64, v250
	v_med3_f32 v5, v5, s64, v250
	v_med3_f32 v6, v6, s64, v250
	v_med3_f32 v7, v7, s64, v250
	v_med3_f32 v8, v8, s64, v250
	v_med3_f32 v9, v9, s64, v250
	v_med3_f32 v10, v10, s64, v250
	v_med3_f32 v11, v11, s64, v250
	v_cvt_pk_fp8_f32 v12, v4, v5
	v_cvt_pk_fp8_f32 v13, v8, v9
	s_nop 0
	v_cvt_pk_fp8_f32 v12, v6, v7 op_sel:[0,0,1]
	v_cvt_pk_fp8_f32 v13, v10, v11 op_sel:[0,0,1]
	v_add_u32_e32 v18, 0x90, v0
	v_mad_i64_i32 v[18:19], s[22:23], v18, s73, v[2:3]
	global_store_dwordx2 v[18:19], v[12:13], off
	v_pk_mul_f32 v[4:5], v[62:63], v[14:15] op_sel_hi:[1,0]
	v_pk_mul_f32 v[6:7], v[64:65], v[14:15] op_sel_hi:[1,0]
	v_pk_mul_f32 v[8:9], v[54:55], v[14:15] op_sel_hi:[1,0]
	v_pk_mul_f32 v[10:11], v[56:57], v[14:15] op_sel_hi:[1,0]
	v_exp_f32_e32 v4, v4
	v_exp_f32_e32 v5, v5
	v_exp_f32_e32 v6, v6
	v_exp_f32_e32 v7, v7
	v_exp_f32_e32 v8, v8
	v_exp_f32_e32 v9, v9
	v_exp_f32_e32 v10, v10
	v_exp_f32_e32 v11, v11
	v_pk_add_f32 v[4:5], v[4:5], v[20:21] op_sel_hi:[1,0]
	v_pk_add_f32 v[6:7], v[6:7], v[20:21] op_sel_hi:[1,0]
	v_pk_add_f32 v[8:9], v[8:9], v[20:21] op_sel_hi:[1,0]
	v_pk_add_f32 v[10:11], v[10:11], v[20:21] op_sel_hi:[1,0]
	v_rcp_f32_e32 v4, v4
	v_rcp_f32_e32 v5, v5
	v_rcp_f32_e32 v6, v6
	v_rcp_f32_e32 v7, v7
	v_rcp_f32_e32 v8, v8
	v_rcp_f32_e32 v9, v9
	v_rcp_f32_e32 v10, v10
	v_rcp_f32_e32 v11, v11
	v_pk_mul_f32 v[4:5], v[62:63], v[4:5]
	v_pk_mul_f32 v[6:7], v[64:65], v[6:7]
	v_pk_mul_f32 v[8:9], v[54:55], v[8:9]
	v_pk_mul_f32 v[10:11], v[56:57], v[10:11]
	v_pk_mul_f32 v[4:5], v[58:59], v[4:5]
	v_pk_mul_f32 v[6:7], v[60:61], v[6:7]
	v_pk_mul_f32 v[8:9], v[50:51], v[8:9]
	v_pk_mul_f32 v[10:11], v[52:53], v[10:11]
	v_med3_f32 v4, v4, s64, v250
	v_med3_f32 v5, v5, s64, v250
	v_med3_f32 v6, v6, s64, v250
	v_med3_f32 v7, v7, s64, v250
	v_med3_f32 v8, v8, s64, v250
	v_med3_f32 v9, v9, s64, v250
	v_med3_f32 v10, v10, s64, v250
	v_med3_f32 v11, v11, s64, v250
	v_cvt_pk_fp8_f32 v12, v4, v5
	v_cvt_pk_fp8_f32 v13, v8, v9
	s_nop 0
	v_cvt_pk_fp8_f32 v12, v6, v7 op_sel:[0,0,1]
	v_cvt_pk_fp8_f32 v13, v10, v11 op_sel:[0,0,1]
	v_add_u32_e32 v18, 0xa0, v0
	v_mad_i64_i32 v[18:19], s[22:23], v18, s73, v[2:3]
	global_store_dwordx2 v[18:19], v[12:13], off
	v_pk_mul_f32 v[4:5], v[46:47], v[14:15] op_sel_hi:[1,0]
	v_pk_mul_f32 v[6:7], v[48:49], v[14:15] op_sel_hi:[1,0]
	v_pk_mul_f32 v[8:9], v[38:39], v[14:15] op_sel_hi:[1,0]
	v_pk_mul_f32 v[10:11], v[40:41], v[14:15] op_sel_hi:[1,0]
	v_exp_f32_e32 v4, v4
	v_exp_f32_e32 v5, v5
	v_exp_f32_e32 v6, v6
	v_exp_f32_e32 v7, v7
	v_exp_f32_e32 v8, v8
	v_exp_f32_e32 v9, v9
	v_exp_f32_e32 v10, v10
	v_exp_f32_e32 v11, v11
	v_pk_add_f32 v[4:5], v[4:5], v[20:21] op_sel_hi:[1,0]
	v_pk_add_f32 v[6:7], v[6:7], v[20:21] op_sel_hi:[1,0]
	v_pk_add_f32 v[8:9], v[8:9], v[20:21] op_sel_hi:[1,0]
	v_pk_add_f32 v[10:11], v[10:11], v[20:21] op_sel_hi:[1,0]
	v_rcp_f32_e32 v4, v4
	v_rcp_f32_e32 v5, v5
	v_rcp_f32_e32 v6, v6
	v_rcp_f32_e32 v7, v7
	v_rcp_f32_e32 v8, v8
	v_rcp_f32_e32 v9, v9
	v_rcp_f32_e32 v10, v10
	v_rcp_f32_e32 v11, v11
	v_pk_mul_f32 v[4:5], v[46:47], v[4:5]
	v_pk_mul_f32 v[6:7], v[48:49], v[6:7]
	v_pk_mul_f32 v[8:9], v[38:39], v[8:9]
	v_pk_mul_f32 v[10:11], v[40:41], v[10:11]
	v_pk_mul_f32 v[4:5], v[42:43], v[4:5]
	v_pk_mul_f32 v[6:7], v[44:45], v[6:7]
	v_pk_mul_f32 v[8:9], v[34:35], v[8:9]
	v_pk_mul_f32 v[10:11], v[36:37], v[10:11]
	v_med3_f32 v4, v4, s64, v250
	v_med3_f32 v5, v5, s64, v250
	v_med3_f32 v6, v6, s64, v250
	v_med3_f32 v7, v7, s64, v250
	v_med3_f32 v8, v8, s64, v250
	v_med3_f32 v9, v9, s64, v250
	v_med3_f32 v10, v10, s64, v250
	v_med3_f32 v11, v11, s64, v250
	v_cvt_pk_fp8_f32 v12, v4, v5
	v_cvt_pk_fp8_f32 v13, v8, v9
	s_nop 0
	v_cvt_pk_fp8_f32 v12, v6, v7 op_sel:[0,0,1]
	v_cvt_pk_fp8_f32 v13, v10, v11 op_sel:[0,0,1]
	v_add_u32_e32 v0, 0xb0, v0
	v_mad_i64_i32 v[2:3], s[22:23], v0, s73, v[2:3]
	s_mov_b64 s[22:23], -1
	s_and_b64 vcc, exec, s[2:3]
	global_store_dwordx2 v[2:3], v[12:13], off
	s_cbranch_vccnz .LBB0_1358
	s_andn2_b64 vcc, exec, s[14:15]
	s_cbranch_vccnz .LBB0_1357
	s_barrier
	s_branch .LBB0_1357
